# v56 + code placement: all eight GEMM K-loop heads on 64-byte boundaries (.p2align 6)
# speedup vs baseline: 1.0056x; 1.0056x over previous
; #define PG8_STAGE(bufoff, gbase, voff) do { _Pragma("unroll") for (int _i = 0; _i < 2; ++_i) \
;         __builtin_amdgcn_global_load_lds((const unsigned*)((const char*)(gbase) + (voff)[_i]), (PG8_LAS unsigned*)(lds + (bufoff) + ldsw + _i * 8192), 16, 0, 0); } while (0)
; #define PG8_LDA(dst, b, h) do { _Pragma("unroll") for (int m = 0; m < 4; ++m) _Pragma("unroll") for (int k = 0; k < 2; ++k) dst[m][k] = *(const PG8_LAS bf16x8*)(lds + PG8_SA(b, h) + aoff + m * 2048 + k * 1024); } while (0)
; #define PG8_LDB(dst, b, h) do { _Pragma("unroll") for (int n = 0; n < 2; ++n) _Pragma("unroll") for (int k = 0; k < 2; ++k) dst[n][k] = *(const PG8_LAS bf16x8*)(lds + PG8_SB(b, h) + boff + n * 2048 + k * 1024); } while (0)
; #define PG8_MMA(ai, bj, At, Bt) do { __builtin_amdgcn_s_setprio(1); _Pragma("unroll") for (int m = 0; m < 4; ++m) _Pragma("unroll") for (int n = 0; n < 2; ++n) _Pragma("unroll") for (int k = 0; k < 2; ++k) \
;         acc[ai][bj][m][n] = __builtin_amdgcn_mfma_f32_16x16x32_bf16(Bt[n][k], At[m][k], acc[ai][bj][m][n], 0, 0, 0); __builtin_amdgcn_s_setprio(0); } while (0)
; #define PG8_WAIT_V(n) asm volatile("s_waitcnt vmcnt(" #n ")" ::: "memory")
; #define PG8_WAIT_L(n) asm volatile("s_waitcnt lgkmcnt(" #n ")" ::: "memory")
; #define PG8_BAR __builtin_amdgcn_s_barrier()
; #define PG8_SCHED __builtin_amdgcn_sched_barrier(0)
; template <class Epi, class Sched, bool ALIGN_EPI = false, bool SP2 = false>
; __device__ __forceinline__ void gemm_phase(PG8_LAS unsigned char* lds, const Gemm g, const Sched& S, const Epi& E) {
;     ...
;             PG8_LDB(B0, 0, 0); PG8_LDB(B1, 0, 1); PG8_SCHED; PG8_LDA(At, 0, 0); PG8_STAGE(PG8_SA(1, 1), a1 + hstepA, voffA);
;             PG8_WAIT_V(8); PG8_WAIT_L(0); PG8_BAR; PG8_MMA(0, 0, At, B0); PG8_MMA(0, 1, At, B1); PG8_BAR; PG8_SCHED;
;             PG8_LDA(At, 0, 1); PG8_STAGE(PG8_SB(0, 0), b2, voffB); PG8_STAGE(PG8_SB(0, 1), b2 + hstepB, voffB); PG8_STAGE(PG8_SA(0, 0), a2, voffA);
;             PG8_WAIT_V(8); PG8_WAIT_L(0); PG8_BAR; PG8_MMA(1, 0, At, B0); PG8_MMA(1, 1, At, B1); PG8_BAR; PG8_SCHED;
.LBB0_152:
	s_ashr_i32 s15, s14, 31
	s_lshl_b64 s[16:17], s[14:15], 19
	s_add_u32 s16, s31, s16
	s_addc_u32 s17, s33, s17
	s_and_b64 s[18:19], s[2:3], exec
	s_cselect_b32 s15, s17, s25
	s_cselect_b32 s49, s16, s24
	s_ashr_i32 s13, s12, 31
	s_lshl_b64 s[18:19], s[12:13], 19
	s_add_u32 s18, s34, s18
	s_addc_u32 s19, s35, s19
	s_and_b64 s[26:27], s[2:3], exec
	s_cselect_b32 s13, s19, s23
	s_cselect_b32 s50, s18, s22
	s_add_u32 s51, s22, 0x100
	s_addc_u32 s52, s23, 0
	s_add_u32 s22, s24, 0x40080
	s_addc_u32 s23, s25, 0
	s_mov_b32 s53, -2
	s_add_u32 s24, s22, 0xfffc0080
	s_addc_u32 s25, s23, -1
	s_add_i32 s54, 0, 0x10000
	s_cmp_eq_u32 s53, 12
	s_cselect_b32 s27, s15, s25
	s_cselect_b32 s26, s49, s24
	v_add_u32_e32 v144, s54, v147
	s_cselect_b32 s25, s13, s52
	s_cselect_b32 s24, s50, s51
	s_add_i32 s56, 0, 0x14000
	ds_read_b128 v[150:153], v144
	ds_read_b128 v[154:157], v144 offset:1024
	ds_read_b128 v[158:161], v144 offset:2048
	ds_read_b128 v[162:165], v144 offset:3072
	v_add_u32_e32 v144, s56, v147
	ds_read_b128 v[166:169], v144
	ds_read_b128 v[170:173], v144 offset:1024
	ds_read_b128 v[174:177], v144 offset:2048
	ds_read_b128 v[178:181], v144 offset:3072
	v_lshl_add_u64 v[144:145], s[22:23], 0, v[142:143]
	s_add_i32 m0, s41, 0xc000
	ds_read_b128 v[182:185], v149
	ds_read_b128 v[186:189], v149 offset:1024
	ds_read_b128 v[190:193], v149 offset:2048
	ds_read_b128 v[194:197], v149 offset:3072
	ds_read_b128 v[210:213], v149 offset:4096
	ds_read_b128 v[226:229], v149 offset:5120
	ds_read_b128 v[230:233], v149 offset:6144
	ds_read_b128 v[234:237], v149 offset:7168
	v_lshl_add_u64 v[244:245], v[240:241], 0, s[64:65]
	s_mov_b32 m0, s45
	s_nop 0
	global_load_lds_dwordx4 v[244:245], off
	v_lshl_add_u64 v[244:245], v[242:243], 0, s[64:65]
	s_mov_b32 m0, s46
	s_nop 0
	global_load_lds_dwordx4 v[244:245], off
	s_add_i32 m0, s41, 0xc000
	s_nop 0
	global_load_lds_dwordx4 v[144:145], off
	v_lshl_add_u64 v[144:145], s[22:23], 0, v[140:141]
	s_add_i32 m0, s41, 0xe000
	s_nop 0
	global_load_lds_dwordx4 v[144:145], off
	s_waitcnt vmcnt(8)
	s_waitcnt lgkmcnt(0)
	s_barrier
	s_setprio 1
	s_waitcnt lgkmcnt(0)
	v_mfma_f32_16x16x32_bf16 v[128:131], v[150:153], v[182:185], 0
	v_mfma_f32_16x16x32_bf16 v[120:123], v[158:161], v[182:185], 0
	v_mfma_f32_16x16x32_bf16 v[112:115], v[150:153], v[190:193], 0
	v_mfma_f32_16x16x32_bf16 v[104:107], v[158:161], v[190:193], 0
	v_mfma_f32_16x16x32_bf16 v[96:99], v[150:153], v[210:213], 0
	v_mfma_f32_16x16x32_bf16 v[88:91], v[158:161], v[210:213], 0
	v_mfma_f32_16x16x32_bf16 v[80:83], v[150:153], v[230:233], 0
	v_mfma_f32_16x16x32_bf16 v[72:75], v[158:161], v[230:233], 0
	v_mfma_f32_16x16x32_bf16 v[128:131], v[154:157], v[186:189], v[128:131]
	v_mfma_f32_16x16x32_bf16 v[120:123], v[162:165], v[186:189], v[120:123]
	v_mfma_f32_16x16x32_bf16 v[112:115], v[154:157], v[194:197], v[112:115]
	v_mfma_f32_16x16x32_bf16 v[104:107], v[162:165], v[194:197], v[104:107]
	v_mfma_f32_16x16x32_bf16 v[96:99], v[154:157], v[226:229], v[96:99]
	v_mfma_f32_16x16x32_bf16 v[88:91], v[162:165], v[226:229], v[88:91]
	v_mfma_f32_16x16x32_bf16 v[80:83], v[154:157], v[234:237], v[80:83]
	v_mfma_f32_16x16x32_bf16 v[72:75], v[162:165], v[234:237], v[72:75]
	s_setprio 0
	s_setprio 1
	v_mfma_f32_16x16x32_bf16 v[124:127], v[166:169], v[182:185], 0
	v_mfma_f32_16x16x32_bf16 v[116:119], v[174:177], v[182:185], 0
	v_mfma_f32_16x16x32_bf16 v[108:111], v[166:169], v[190:193], 0
	v_mfma_f32_16x16x32_bf16 v[100:103], v[174:177], v[190:193], 0
	v_mfma_f32_16x16x32_bf16 v[92:95], v[166:169], v[210:213], 0
	v_mfma_f32_16x16x32_bf16 v[84:87], v[174:177], v[210:213], 0
	v_mfma_f32_16x16x32_bf16 v[76:79], v[166:169], v[230:233], 0
	v_mfma_f32_16x16x32_bf16 v[68:71], v[174:177], v[230:233], 0
	v_mfma_f32_16x16x32_bf16 v[124:127], v[170:173], v[186:189], v[124:127]
	v_mfma_f32_16x16x32_bf16 v[116:119], v[178:181], v[186:189], v[116:119]
	v_mfma_f32_16x16x32_bf16 v[108:111], v[170:173], v[194:197], v[108:111]
	v_mfma_f32_16x16x32_bf16 v[100:103], v[178:181], v[194:197], v[100:103]
	v_mfma_f32_16x16x32_bf16 v[92:95], v[170:173], v[226:229], v[92:95]
	v_mfma_f32_16x16x32_bf16 v[84:87], v[178:181], v[226:229], v[84:87]
	v_mfma_f32_16x16x32_bf16 v[76:79], v[170:173], v[234:237], v[76:79]
	v_mfma_f32_16x16x32_bf16 v[68:71], v[178:181], v[234:237], v[68:71]
	s_setprio 0
	s_barrier
	s_add_i32 s54, s54, s39
	v_lshl_add_u64 v[144:145], s[24:25], 0, v[136:137]
	s_mov_b32 m0, s54
	ds_read_b128 v[182:185], v149 offset:16384
	ds_read_b128 v[186:189], v149 offset:17408
	ds_read_b128 v[190:193], v149 offset:18432
	ds_read_b128 v[194:197], v149 offset:19456
	ds_read_b128 v[210:213], v149 offset:20480
	ds_read_b128 v[226:229], v149 offset:21504
	ds_read_b128 v[230:233], v149 offset:22528
	ds_read_b128 v[234:237], v149 offset:23552
	global_load_lds_dwordx4 v[144:145], off
	s_add_i32 m0, s54, 0x2000
	s_add_u32 s54, s24, 0x40000
	v_lshl_add_u64 v[238:239], s[24:25], 0, v[132:133]
	s_addc_u32 s55, s25, 0
	s_add_i32 s56, s56, s39
	global_load_lds_dwordx4 v[238:239], off
	v_lshl_add_u64 v[240:241], s[54:55], 0, v[136:137]
	s_mov_b32 m0, s56
	v_lshl_add_u64 v[242:243], s[26:27], 0, v[134:135]
	global_load_lds_dwordx4 v[240:241], off
	v_lshl_add_u64 v[240:241], s[54:55], 0, v[132:133]
	s_add_i32 m0, s56, 0x2000
	s_nop 0
	global_load_lds_dwordx4 v[240:241], off
	v_lshl_add_u64 v[240:241], s[26:27], 0, v[138:139]
	s_waitcnt vmcnt(6)
	s_waitcnt lgkmcnt(0)
	s_barrier
; #define PG8_STAGE(bufoff, gbase, voff) do { _Pragma("unroll") for (int _i = 0; _i < 2; ++_i) \
;         __builtin_amdgcn_global_load_lds((const unsigned*)((const char*)(gbase) + (voff)[_i]), (PG8_LAS unsigned*)(lds + (bufoff) + ldsw + _i * 8192), 16, 0, 0); } while (0)
; #define PG8_LDA(dst, b, h) do { _Pragma("unroll") for (int m = 0; m < 4; ++m) _Pragma("unroll") for (int k = 0; k < 2; ++k) dst[m][k] = *(const PG8_LAS bf16x8*)(lds + PG8_SA(b, h) + aoff + m * 2048 + k * 1024); } while (0)
; #define PG8_LDB(dst, b, h) do { _Pragma("unroll") for (int n = 0; n < 2; ++n) _Pragma("unroll") for (int k = 0; k < 2; ++k) dst[n][k] = *(const PG8_LAS bf16x8*)(lds + PG8_SB(b, h) + boff + n * 2048 + k * 1024); } while (0)
; #define PG8_MMA(ai, bj, At, Bt) do { __builtin_amdgcn_s_setprio(1); _Pragma("unroll") for (int m = 0; m < 4; ++m) _Pragma("unroll") for (int n = 0; n < 2; ++n) _Pragma("unroll") for (int k = 0; k < 2; ++k) \
;         acc[ai][bj][m][n] = __builtin_amdgcn_mfma_f32_16x16x32_bf16(Bt[n][k], At[m][k], acc[ai][bj][m][n], 0, 0, 0); __builtin_amdgcn_s_setprio(0); } while (0)
; #define PG8_WAIT_V(n) asm volatile("s_waitcnt vmcnt(" #n ")" ::: "memory")
; #define PG8_WAIT_L(n) asm volatile("s_waitcnt lgkmcnt(" #n ")" ::: "memory")
; #define PG8_BAR __builtin_amdgcn_s_barrier()
; #define PG8_SCHED __builtin_amdgcn_sched_barrier(0)
; template <class Epi, class Sched, bool ALIGN_EPI = false, bool SP2 = false>
; __device__ __forceinline__ void gemm_phase(PG8_LAS unsigned char* lds, const Gemm g, const Sched& S, const Epi& E) {
;     ...
;             PG8_WAIT_V(8); PG8_WAIT_L(0); PG8_BAR; PG8_MMA(1, 0, At, B0); PG8_MMA(1, 1, At, B1); PG8_BAR; PG8_SCHED;
;             PG8_LDB(B0, 1, 0); PG8_LDB(B1, 1, 1); PG8_SCHED; PG8_LDA(At, 1, 0); PG8_STAGE(PG8_SA(0, 1), a2 + hstepA, voffA);
;             PG8_WAIT_V(8); PG8_WAIT_L(0); PG8_BAR; PG8_MMA(0, 0, At, B0); PG8_MMA(0, 1, At, B1); PG8_BAR; PG8_SCHED;
	s_setprio 1
	s_waitcnt lgkmcnt(0)
	v_mfma_f32_16x16x32_bf16 v[64:67], v[150:153], v[182:185], 0
	v_mfma_f32_16x16x32_bf16 v[56:59], v[158:161], v[182:185], 0
	v_mfma_f32_16x16x32_bf16 v[48:51], v[150:153], v[190:193], 0
	v_mfma_f32_16x16x32_bf16 v[40:43], v[158:161], v[190:193], 0
	v_mfma_f32_16x16x32_bf16 v[32:35], v[150:153], v[210:213], 0
	v_mfma_f32_16x16x32_bf16 v[24:27], v[158:161], v[210:213], 0
	v_mfma_f32_16x16x32_bf16 v[16:19], v[150:153], v[230:233], 0
	v_mfma_f32_16x16x32_bf16 v[8:11], v[158:161], v[230:233], 0
	v_mfma_f32_16x16x32_bf16 v[64:67], v[154:157], v[186:189], v[64:67]
	v_mfma_f32_16x16x32_bf16 v[56:59], v[162:165], v[186:189], v[56:59]
	v_mfma_f32_16x16x32_bf16 v[48:51], v[154:157], v[194:197], v[48:51]
	v_mfma_f32_16x16x32_bf16 v[40:43], v[162:165], v[194:197], v[40:43]
	v_mfma_f32_16x16x32_bf16 v[32:35], v[154:157], v[226:229], v[32:35]
	v_mfma_f32_16x16x32_bf16 v[24:27], v[162:165], v[226:229], v[24:27]
	v_mfma_f32_16x16x32_bf16 v[16:19], v[154:157], v[234:237], v[16:19]
	v_mfma_f32_16x16x32_bf16 v[8:11], v[162:165], v[234:237], v[8:11]
	s_setprio 0
	s_setprio 1
	v_mfma_f32_16x16x32_bf16 v[60:63], v[166:169], v[182:185], 0
	v_mfma_f32_16x16x32_bf16 v[52:55], v[174:177], v[182:185], 0
	v_mfma_f32_16x16x32_bf16 v[44:47], v[166:169], v[190:193], 0
	v_mfma_f32_16x16x32_bf16 v[36:39], v[174:177], v[190:193], 0
	v_mfma_f32_16x16x32_bf16 v[28:31], v[166:169], v[210:213], 0
	v_mfma_f32_16x16x32_bf16 v[20:23], v[174:177], v[210:213], 0
	v_mfma_f32_16x16x32_bf16 v[12:15], v[166:169], v[230:233], 0
	v_mfma_f32_16x16x32_bf16 v[4:7], v[174:177], v[230:233], 0
	v_mfma_f32_16x16x32_bf16 v[60:63], v[170:173], v[186:189], v[60:63]
	v_mfma_f32_16x16x32_bf16 v[52:55], v[178:181], v[186:189], v[52:55]
	v_mfma_f32_16x16x32_bf16 v[44:47], v[170:173], v[194:197], v[44:47]
	v_mfma_f32_16x16x32_bf16 v[36:39], v[178:181], v[194:197], v[36:39]
	v_mfma_f32_16x16x32_bf16 v[28:31], v[170:173], v[226:229], v[28:31]
	v_mfma_f32_16x16x32_bf16 v[20:23], v[178:181], v[226:229], v[20:23]
	v_mfma_f32_16x16x32_bf16 v[12:15], v[170:173], v[234:237], v[12:15]
	v_mfma_f32_16x16x32_bf16 v[4:7], v[178:181], v[234:237], v[4:7]
	s_setprio 0
	s_barrier
	s_add_i32 s54, 0, 0x18000
	s_add_i32 s55, 0, 0x1c000
	v_add_u32_e32 v162, s54, v147
	v_add_u32_e32 v178, s55, v147
	ds_read_b128 v[150:153], v162
	ds_read_b128 v[154:157], v162 offset:1024
	ds_read_b128 v[158:161], v162 offset:2048
	ds_read_b128 v[162:165], v162 offset:3072
	ds_read_b128 v[166:169], v178
	ds_read_b128 v[170:173], v178 offset:1024
	ds_read_b128 v[174:177], v178 offset:2048
	ds_read_b128 v[178:181], v178 offset:3072
	s_add_u32 s26, s26, 0x40000
	s_addc_u32 s27, s27, 0
	s_mov_b32 m0, s43
	v_lshl_add_u64 v[244:245], s[26:27], 0, v[138:139]
	ds_read_b128 v[182:185], v149 offset:32768
	ds_read_b128 v[186:189], v149 offset:33792
	ds_read_b128 v[190:193], v149 offset:34816
	ds_read_b128 v[194:197], v149 offset:35840
	ds_read_b128 v[210:213], v149 offset:36864
	ds_read_b128 v[226:229], v149 offset:37888
	ds_read_b128 v[230:233], v149 offset:38912
	ds_read_b128 v[234:237], v149 offset:39936
	s_mov_b32 m0, s41
	s_nop 0
	global_load_lds_dwordx4 v[240:241], off
	s_mov_b32 m0, s42
	s_nop 0
	global_load_lds_dwordx4 v[242:243], off
	s_mov_b32 m0, s43
	s_nop 0
	global_load_lds_dwordx4 v[244:245], off
	v_lshl_add_u64 v[244:245], s[26:27], 0, v[134:135]
	s_mov_b32 m0, s44
	s_nop 0
	global_load_lds_dwordx4 v[244:245], off
	s_waitcnt vmcnt(8)
	s_waitcnt lgkmcnt(0)
	s_barrier
; #define PG8_STAGE(bufoff, gbase, voff) do { _Pragma("unroll") for (int _i = 0; _i < 2; ++_i) \
;         __builtin_amdgcn_global_load_lds((const unsigned*)((const char*)(gbase) + (voff)[_i]), (PG8_LAS unsigned*)(lds + (bufoff) + ldsw + _i * 8192), 16, 0, 0); } while (0)
; #define PG8_LDA(dst, b, h) do { _Pragma("unroll") for (int m = 0; m < 4; ++m) _Pragma("unroll") for (int k = 0; k < 2; ++k) dst[m][k] = *(const PG8_LAS bf16x8*)(lds + PG8_SA(b, h) + aoff + m * 2048 + k * 1024); } while (0)
; #define PG8_MMA(ai, bj, At, Bt) do { __builtin_amdgcn_s_setprio(1); _Pragma("unroll") for (int m = 0; m < 4; ++m) _Pragma("unroll") for (int n = 0; n < 2; ++n) _Pragma("unroll") for (int k = 0; k < 2; ++k) \
;         acc[ai][bj][m][n] = __builtin_amdgcn_mfma_f32_16x16x32_bf16(Bt[n][k], At[m][k], acc[ai][bj][m][n], 0, 0, 0); __builtin_amdgcn_s_setprio(0); } while (0)
; #define PG8_WAIT_V(n) asm volatile("s_waitcnt vmcnt(" #n ")" ::: "memory")
; #define PG8_WAIT_L(n) asm volatile("s_waitcnt lgkmcnt(" #n ")" ::: "memory")
; #define PG8_BAR __builtin_amdgcn_s_barrier()
; #define PG8_SCHED __builtin_amdgcn_sched_barrier(0)
; template <class Epi, class Sched, bool ALIGN_EPI = false, bool SP2 = false>
; __device__ __forceinline__ void gemm_phase(PG8_LAS unsigned char* lds, const Gemm g, const Sched& S, const Epi& E) {
;     ...
;         for (int t = 0; t < nt; t += 2) {
;     ...
;             PG8_WAIT_V(8); PG8_WAIT_L(0); PG8_BAR; PG8_MMA(0, 0, At, B0); PG8_MMA(0, 1, At, B1); PG8_BAR; PG8_SCHED;
;             PG8_LDA(At, 1, 1); PG8_STAGE(PG8_SB(1, 0), b3, voffB); PG8_STAGE(PG8_SB(1, 1), b3 + hstepB, voffB); PG8_STAGE(PG8_SA(1, 0), a3, voffA);
;             PG8_WAIT_V(8); PG8_WAIT_L(0); PG8_BAR; PG8_MMA(1, 0, At, B0); PG8_MMA(1, 1, At, B1); PG8_BAR; PG8_SCHED;
	s_setprio 1
	s_waitcnt lgkmcnt(0)
	v_mfma_f32_16x16x32_bf16 v[128:131], v[150:153], v[182:185], v[128:131]
	v_mfma_f32_16x16x32_bf16 v[120:123], v[158:161], v[182:185], v[120:123]
	v_mfma_f32_16x16x32_bf16 v[112:115], v[150:153], v[190:193], v[112:115]
	v_mfma_f32_16x16x32_bf16 v[104:107], v[158:161], v[190:193], v[104:107]
	v_mfma_f32_16x16x32_bf16 v[96:99], v[150:153], v[210:213], v[96:99]
	v_mfma_f32_16x16x32_bf16 v[88:91], v[158:161], v[210:213], v[88:91]
	v_mfma_f32_16x16x32_bf16 v[80:83], v[150:153], v[230:233], v[80:83]
	v_mfma_f32_16x16x32_bf16 v[72:75], v[158:161], v[230:233], v[72:75]
	v_mfma_f32_16x16x32_bf16 v[128:131], v[154:157], v[186:189], v[128:131]
	v_mfma_f32_16x16x32_bf16 v[120:123], v[162:165], v[186:189], v[120:123]
	v_mfma_f32_16x16x32_bf16 v[112:115], v[154:157], v[194:197], v[112:115]
	v_mfma_f32_16x16x32_bf16 v[104:107], v[162:165], v[194:197], v[104:107]
	v_mfma_f32_16x16x32_bf16 v[96:99], v[154:157], v[226:229], v[96:99]
	v_mfma_f32_16x16x32_bf16 v[88:91], v[162:165], v[226:229], v[88:91]
	v_mfma_f32_16x16x32_bf16 v[80:83], v[154:157], v[234:237], v[80:83]
	v_mfma_f32_16x16x32_bf16 v[72:75], v[162:165], v[234:237], v[72:75]
	s_setprio 0
	s_setprio 1
	v_mfma_f32_16x16x32_bf16 v[124:127], v[166:169], v[182:185], v[124:127]
	v_mfma_f32_16x16x32_bf16 v[116:119], v[174:177], v[182:185], v[116:119]
	v_mfma_f32_16x16x32_bf16 v[108:111], v[166:169], v[190:193], v[108:111]
	v_mfma_f32_16x16x32_bf16 v[100:103], v[174:177], v[190:193], v[100:103]
	v_mfma_f32_16x16x32_bf16 v[92:95], v[166:169], v[210:213], v[92:95]
	v_mfma_f32_16x16x32_bf16 v[84:87], v[174:177], v[210:213], v[84:87]
	v_mfma_f32_16x16x32_bf16 v[76:79], v[166:169], v[230:233], v[76:79]
	v_mfma_f32_16x16x32_bf16 v[68:71], v[174:177], v[230:233], v[68:71]
	v_mfma_f32_16x16x32_bf16 v[124:127], v[170:173], v[186:189], v[124:127]
	v_mfma_f32_16x16x32_bf16 v[116:119], v[178:181], v[186:189], v[116:119]
	v_mfma_f32_16x16x32_bf16 v[108:111], v[170:173], v[194:197], v[108:111]
	v_mfma_f32_16x16x32_bf16 v[100:103], v[178:181], v[194:197], v[100:103]
	v_mfma_f32_16x16x32_bf16 v[92:95], v[170:173], v[226:229], v[92:95]
	v_mfma_f32_16x16x32_bf16 v[84:87], v[178:181], v[226:229], v[84:87]
	v_mfma_f32_16x16x32_bf16 v[76:79], v[170:173], v[234:237], v[76:79]
	v_mfma_f32_16x16x32_bf16 v[68:71], v[178:181], v[234:237], v[68:71]
	s_setprio 0
	s_barrier
	s_add_i32 s26, s54, s39
	v_lshl_add_u64 v[144:145], v[144:145], 0, s[64:65]
	s_mov_b32 m0, s26
	ds_read_b128 v[182:185], v149 offset:49152
	ds_read_b128 v[186:189], v149 offset:50176
	ds_read_b128 v[190:193], v149 offset:51200
	ds_read_b128 v[194:197], v149 offset:52224
	ds_read_b128 v[210:213], v149 offset:53248
	ds_read_b128 v[226:229], v149 offset:54272
	ds_read_b128 v[230:233], v149 offset:55296
	ds_read_b128 v[234:237], v149 offset:56320
	global_load_lds_dwordx4 v[144:145], off
	s_add_i32 m0, s26, 0x2000
	s_add_u32 s24, s24, 0x40080
	v_lshl_add_u64 v[144:145], v[238:239], 0, s[64:65]
	s_addc_u32 s25, s25, 0
	s_add_i32 s26, s55, s39
	global_load_lds_dwordx4 v[144:145], off
	v_lshl_add_u64 v[144:145], s[24:25], 0, v[136:137]
	s_mov_b32 m0, s26
	s_nop 0
	global_load_lds_dwordx4 v[144:145], off
	v_lshl_add_u64 v[144:145], s[24:25], 0, v[132:133]
	s_add_i32 m0, s26, 0x2000
	s_nop 0
	global_load_lds_dwordx4 v[144:145], off
	s_waitcnt vmcnt(6)
	s_waitcnt lgkmcnt(0)
	s_barrier
	s_setprio 1
	s_waitcnt lgkmcnt(0)
	v_mfma_f32_16x16x32_bf16 v[64:67], v[150:153], v[182:185], v[64:67]
	v_mfma_f32_16x16x32_bf16 v[56:59], v[158:161], v[182:185], v[56:59]
	v_mfma_f32_16x16x32_bf16 v[48:51], v[150:153], v[190:193], v[48:51]
	v_mfma_f32_16x16x32_bf16 v[40:43], v[158:161], v[190:193], v[40:43]
	v_mfma_f32_16x16x32_bf16 v[32:35], v[150:153], v[210:213], v[32:35]
	v_mfma_f32_16x16x32_bf16 v[24:27], v[158:161], v[210:213], v[24:27]
	v_mfma_f32_16x16x32_bf16 v[16:19], v[150:153], v[230:233], v[16:19]
	v_mfma_f32_16x16x32_bf16 v[8:11], v[158:161], v[230:233], v[8:11]
	v_mfma_f32_16x16x32_bf16 v[64:67], v[154:157], v[186:189], v[64:67]
	v_mfma_f32_16x16x32_bf16 v[56:59], v[162:165], v[186:189], v[56:59]
	v_mfma_f32_16x16x32_bf16 v[48:51], v[154:157], v[194:197], v[48:51]
	v_mfma_f32_16x16x32_bf16 v[40:43], v[162:165], v[194:197], v[40:43]
	v_mfma_f32_16x16x32_bf16 v[32:35], v[154:157], v[226:229], v[32:35]
	v_mfma_f32_16x16x32_bf16 v[24:27], v[162:165], v[226:229], v[24:27]
	v_mfma_f32_16x16x32_bf16 v[16:19], v[154:157], v[234:237], v[16:19]
	v_mfma_f32_16x16x32_bf16 v[8:11], v[162:165], v[234:237], v[8:11]
	s_setprio 0
	s_setprio 1
	v_mfma_f32_16x16x32_bf16 v[60:63], v[166:169], v[182:185], v[60:63]
	v_mfma_f32_16x16x32_bf16 v[52:55], v[174:177], v[182:185], v[52:55]
	v_mfma_f32_16x16x32_bf16 v[44:47], v[166:169], v[190:193], v[44:47]
	v_mfma_f32_16x16x32_bf16 v[36:39], v[174:177], v[190:193], v[36:39]
	v_mfma_f32_16x16x32_bf16 v[28:31], v[166:169], v[210:213], v[28:31]
	v_mfma_f32_16x16x32_bf16 v[20:23], v[174:177], v[210:213], v[20:23]
	v_mfma_f32_16x16x32_bf16 v[12:15], v[166:169], v[230:233], v[12:15]
	v_mfma_f32_16x16x32_bf16 v[4:7], v[174:177], v[230:233], v[4:7]
	v_mfma_f32_16x16x32_bf16 v[60:63], v[170:173], v[186:189], v[60:63]
	v_mfma_f32_16x16x32_bf16 v[52:55], v[178:181], v[186:189], v[52:55]
	v_mfma_f32_16x16x32_bf16 v[44:47], v[170:173], v[194:197], v[44:47]
	v_mfma_f32_16x16x32_bf16 v[36:39], v[178:181], v[194:197], v[36:39]
	v_mfma_f32_16x16x32_bf16 v[28:31], v[170:173], v[226:229], v[28:31]
	v_mfma_f32_16x16x32_bf16 v[20:23], v[178:181], v[226:229], v[20:23]
	v_mfma_f32_16x16x32_bf16 v[12:15], v[170:173], v[234:237], v[12:15]
	v_mfma_f32_16x16x32_bf16 v[4:7], v[178:181], v[234:237], v[4:7]
	s_setprio 0
	s_barrier
	s_add_i32 s53, s53, 2
	s_add_u32 s51, s51, 0x100
	s_addc_u32 s52, s52, 0
	s_add_u32 s22, s22, 0x100
	s_addc_u32 s23, s23, 0
	s_cmp_gt_u32 s53, 13
	s_cbranch_scc1 .Lpeel_exit_0
	.p2align 6

;     __device__ __forceinline__ bool next(int i, Unit& u) const { const int L = i * G + c; if (L >= 32) return false; u.pm = L; u.pn = L >> 4; return true; }
;     __device__ __forceinline__ bool next(int i, Unit& u) const { if (i != 0) return false; u.pm = pm; u.pn = pn; return true; }
;     __device__ __forceinline__ bool next(int i, Unit& u) const { if (i > 3) return false; u.pm = (i >> 1) * 16 + 2 * x + (i & 1); u.pn = i >> 1; return true; }
; template <class Epi, class Sched, bool ALIGN_EPI = false, bool SP2 = false>
; __device__ __forceinline__ void gemm_phase(PG8_LAS unsigned char* lds, const Gemm g, const Sched& S, const Epi& E) {
;     ...
;         const bool has_next = S.next(ui + 1, nxt);
;         const char* nA = has_next ? (const char*)g.A + (size_t)nxt.pm * tstepA : cA; const char* nB = has_next ? (const char*)g.Bt + (size_t)nxt.pn * tstepB : cB;
;         for (int t = 0; t < nt; t += 2) {
;     ...
; #pragma unroll
;         for (int a = 0; a < 2; ++a)
; #pragma unroll
;             for (int b = 0; b < 2; ++b)
; #pragma unroll
;                 for (int m = 0; m < 4; ++m)
; #pragma unroll
;                     for (int n = 0; n < 2; ++n) acc[a][b][m][n] = (f32x4){0.f, 0.f, 0.f, 0.f};
;         cur = nxt; cA = nA; cB = nB; ++ui;
.LBB0_668:
	s_add_u32 s44, s16, 0x100
	v_mov_b32_e32 v4, 0
	s_addc_u32 s45, s17, 0
	s_mov_b32 s46, -2
	v_mov_b32_e32 v5, v4
	v_mov_b32_e32 v6, v4
	v_mov_b32_e32 v7, v4
	v_mov_b32_e32 v8, v4
	v_mov_b32_e32 v9, v4
	v_mov_b32_e32 v10, v4
	v_mov_b32_e32 v11, v4
	v_mov_b32_e32 v12, v4
	v_mov_b32_e32 v13, v4
	v_mov_b32_e32 v14, v4
	v_mov_b32_e32 v15, v4
	v_mov_b32_e32 v20, v4
	v_mov_b32_e32 v21, v4
	v_mov_b32_e32 v22, v4
	v_mov_b32_e32 v23, v4
	v_mov_b32_e32 v28, v4
	v_mov_b32_e32 v29, v4
	v_mov_b32_e32 v30, v4
	v_mov_b32_e32 v31, v4
	v_mov_b32_e32 v36, v4
	v_mov_b32_e32 v37, v4
	v_mov_b32_e32 v38, v4
	v_mov_b32_e32 v39, v4
	v_mov_b32_e32 v44, v4
	v_mov_b32_e32 v45, v4
	v_mov_b32_e32 v46, v4
	v_mov_b32_e32 v47, v4
	v_mov_b32_e32 v52, v4
	v_mov_b32_e32 v53, v4
	v_mov_b32_e32 v54, v4
	v_mov_b32_e32 v55, v4
	v_mov_b32_e32 v16, v4
	v_mov_b32_e32 v17, v4
	v_mov_b32_e32 v18, v4
	v_mov_b32_e32 v19, v4
	v_mov_b32_e32 v24, v4
	v_mov_b32_e32 v25, v4
	v_mov_b32_e32 v26, v4
	v_mov_b32_e32 v27, v4
	v_mov_b32_e32 v32, v4
	v_mov_b32_e32 v33, v4
	v_mov_b32_e32 v34, v4
	v_mov_b32_e32 v35, v4
	v_mov_b32_e32 v40, v4
	v_mov_b32_e32 v41, v4
	v_mov_b32_e32 v42, v4
	v_mov_b32_e32 v43, v4
	v_mov_b32_e32 v48, v4
	v_mov_b32_e32 v49, v4
	v_mov_b32_e32 v50, v4
	v_mov_b32_e32 v51, v4
	v_mov_b32_e32 v56, v4
	v_mov_b32_e32 v57, v4
	v_mov_b32_e32 v58, v4
	v_mov_b32_e32 v59, v4
	v_mov_b32_e32 v60, v4
	v_mov_b32_e32 v61, v4
	v_mov_b32_e32 v62, v4
	v_mov_b32_e32 v63, v4
	v_mov_b32_e32 v64, v4
	v_mov_b32_e32 v65, v4
	v_mov_b32_e32 v66, v4
	v_mov_b32_e32 v67, v4
	v_mov_b32_e32 v68, v4
	v_mov_b32_e32 v69, v4
	v_mov_b32_e32 v70, v4
	v_mov_b32_e32 v71, v4
	v_mov_b32_e32 v72, v4
	v_mov_b32_e32 v73, v4
	v_mov_b32_e32 v74, v4
	v_mov_b32_e32 v75, v4
	v_mov_b32_e32 v76, v4
	v_mov_b32_e32 v77, v4
	v_mov_b32_e32 v78, v4
	v_mov_b32_e32 v79, v4
	v_mov_b32_e32 v84, v4
	v_mov_b32_e32 v85, v4
	v_mov_b32_e32 v86, v4
	v_mov_b32_e32 v87, v4
	v_mov_b32_e32 v92, v4
	v_mov_b32_e32 v93, v4
	v_mov_b32_e32 v94, v4
	v_mov_b32_e32 v95, v4
	v_mov_b32_e32 v100, v4
	v_mov_b32_e32 v101, v4
	v_mov_b32_e32 v102, v4
	v_mov_b32_e32 v103, v4
	v_mov_b32_e32 v108, v4
	v_mov_b32_e32 v109, v4
	v_mov_b32_e32 v110, v4
	v_mov_b32_e32 v111, v4
	v_mov_b32_e32 v116, v4
	v_mov_b32_e32 v117, v4
	v_mov_b32_e32 v118, v4
	v_mov_b32_e32 v119, v4
	v_mov_b32_e32 v80, v4
	v_mov_b32_e32 v81, v4
	v_mov_b32_e32 v82, v4
	v_mov_b32_e32 v83, v4
	v_mov_b32_e32 v88, v4
	v_mov_b32_e32 v89, v4
	v_mov_b32_e32 v90, v4
	v_mov_b32_e32 v91, v4
	v_mov_b32_e32 v96, v4
	v_mov_b32_e32 v97, v4
	v_mov_b32_e32 v98, v4
	v_mov_b32_e32 v99, v4
	v_mov_b32_e32 v104, v4
	v_mov_b32_e32 v105, v4
	v_mov_b32_e32 v106, v4
	v_mov_b32_e32 v107, v4
	v_mov_b32_e32 v112, v4
	v_mov_b32_e32 v113, v4
	v_mov_b32_e32 v114, v4
	v_mov_b32_e32 v115, v4
	v_mov_b32_e32 v120, v4
	v_mov_b32_e32 v121, v4
	v_mov_b32_e32 v122, v4
	v_mov_b32_e32 v123, v4
	v_mov_b32_e32 v124, v4
	v_mov_b32_e32 v125, v4
	v_mov_b32_e32 v126, v4
	v_mov_b32_e32 v127, v4
	v_mov_b32_e32 v128, v4
	v_mov_b32_e32 v129, v4
	v_mov_b32_e32 v130, v4
	v_mov_b32_e32 v131, v4
	.p2align 6

; #define PG8_STR(x) PG8_STR2(x)
;     __device__ __forceinline__ bool next(int i, Unit& u) const { const int L = i * G + c; if (L >= 32) return false; u.pm = L; u.pn = L >> 4; return true; }
;     __device__ __forceinline__ bool next(int i, Unit& u) const { if (i != 0) return false; u.pm = pm; u.pn = pn; return true; }
;     __device__ __forceinline__ bool next(int i, Unit& u) const { if (i > 3) return false; u.pm = (i >> 1) * 16 + 2 * x + (i & 1); u.pn = i >> 1; return true; }
; template <class Epi, class Sched, bool ALIGN_EPI = false, bool SP2 = false>
; __device__ __forceinline__ void gemm_phase(PG8_LAS unsigned char* lds, const Gemm g, const Sched& S, const Epi& E) {
;     ...
;         const bool has_next = S.next(ui + 1, nxt);
;         const char* nA = has_next ? (const char*)g.A + (size_t)nxt.pm * tstepA : cA; const char* nB = has_next ? (const char*)g.Bt + (size_t)nxt.pn * tstepB : cB;
;         for (int t = 0; t < nt; t += 2) {
;     ...
;             asm volatile(".p2align 6\n\t.rept " PG8_STR(KLOOP_ALIGN) "\n\ts_nop 0\n\t.endr");
;     ...
;             const bool last = (t == nt - 2);
;             const char* a1 = cA + (size_t)(t + 1) * kstep;
;             const char* a2 = last ? nA : cA + (size_t)(t + 2) * kstep; const char* b2 = last ? nB : cB + (size_t)(t + 2) * kstep;
;             const char* a3 = a2 + kstep; const char* b3 = b2 + kstep;
;     ...
; #pragma unroll
;         for (int a = 0; a < 2; ++a)
; #pragma unroll
;             for (int b = 0; b < 2; ++b)
; #pragma unroll
;                 for (int m = 0; m < 4; ++m)
; #pragma unroll
;                     for (int n = 0; n < 2; ++n) acc[a][b][m][n] = (f32x4){0.f, 0.f, 0.f, 0.f};
.LBB0_815:
	s_ashr_i32 s19, s18, 31
	s_lshl_b64 s[20:21], s[18:19], 19
	s_add_u32 s20, s8, s20
	s_addc_u32 s21, s9, s21
	s_and_b64 s[22:23], s[6:7], exec
	s_cselect_b32 s19, s21, s29
	s_cselect_b32 s25, s20, s28
	s_ashr_i32 s17, s16, 31
	s_lshl_b64 s[22:23], s[16:17], 19
	s_add_u32 s22, s10, s22
	s_addc_u32 s23, s11, s23
	s_and_b64 s[30:31], s[6:7], exec
	s_cselect_b32 s17, s23, s27
	s_cselect_b32 s48, s22, s26
	s_add_u32 s49, s26, 0x100
	s_addc_u32 s50, s27, 0
	s_add_u32 s26, s28, 0x40080
	v_mov_b32_e32 v4, 0
	s_addc_u32 s27, s29, 0
	s_mov_b32 s51, -2
	v_mov_b32_e32 v5, v4
	v_mov_b32_e32 v6, v4
	v_mov_b32_e32 v7, v4
	v_mov_b32_e32 v8, v4
	v_mov_b32_e32 v9, v4
	v_mov_b32_e32 v10, v4
	v_mov_b32_e32 v11, v4
	v_mov_b32_e32 v16, v4
	v_mov_b32_e32 v17, v4
	v_mov_b32_e32 v18, v4
	v_mov_b32_e32 v19, v4
	v_mov_b32_e32 v24, v4
	v_mov_b32_e32 v25, v4
	v_mov_b32_e32 v26, v4
	v_mov_b32_e32 v27, v4
	v_mov_b32_e32 v32, v4
	v_mov_b32_e32 v33, v4
	v_mov_b32_e32 v34, v4
	v_mov_b32_e32 v35, v4
	v_mov_b32_e32 v40, v4
	v_mov_b32_e32 v41, v4
	v_mov_b32_e32 v42, v4
	v_mov_b32_e32 v43, v4
	v_mov_b32_e32 v48, v4
	v_mov_b32_e32 v49, v4
	v_mov_b32_e32 v50, v4
	v_mov_b32_e32 v51, v4
	v_mov_b32_e32 v56, v4
	v_mov_b32_e32 v57, v4
	v_mov_b32_e32 v58, v4
	v_mov_b32_e32 v59, v4
	v_mov_b32_e32 v12, v4
	v_mov_b32_e32 v13, v4
	v_mov_b32_e32 v14, v4
	v_mov_b32_e32 v15, v4
	v_mov_b32_e32 v20, v4
	v_mov_b32_e32 v21, v4
	v_mov_b32_e32 v22, v4
	v_mov_b32_e32 v23, v4
	v_mov_b32_e32 v28, v4
	v_mov_b32_e32 v29, v4
	v_mov_b32_e32 v30, v4
	v_mov_b32_e32 v31, v4
	v_mov_b32_e32 v36, v4
	v_mov_b32_e32 v37, v4
	v_mov_b32_e32 v38, v4
	v_mov_b32_e32 v39, v4
	v_mov_b32_e32 v44, v4
	v_mov_b32_e32 v45, v4
	v_mov_b32_e32 v46, v4
	v_mov_b32_e32 v47, v4
	v_mov_b32_e32 v52, v4
	v_mov_b32_e32 v53, v4
	v_mov_b32_e32 v54, v4
	v_mov_b32_e32 v55, v4
	v_mov_b32_e32 v60, v4
	v_mov_b32_e32 v61, v4
	v_mov_b32_e32 v62, v4
	v_mov_b32_e32 v63, v4
	v_mov_b32_e32 v64, v4
	v_mov_b32_e32 v65, v4
	v_mov_b32_e32 v66, v4
	v_mov_b32_e32 v67, v4
	v_mov_b32_e32 v68, v4
	v_mov_b32_e32 v69, v4
	v_mov_b32_e32 v70, v4
	v_mov_b32_e32 v71, v4
	v_mov_b32_e32 v72, v4
	v_mov_b32_e32 v73, v4
	v_mov_b32_e32 v74, v4
	v_mov_b32_e32 v75, v4
	v_mov_b32_e32 v80, v4
	v_mov_b32_e32 v81, v4
	v_mov_b32_e32 v82, v4
	v_mov_b32_e32 v83, v4
	v_mov_b32_e32 v88, v4
	v_mov_b32_e32 v89, v4
	v_mov_b32_e32 v90, v4
	v_mov_b32_e32 v91, v4
	v_mov_b32_e32 v96, v4
	v_mov_b32_e32 v97, v4
	v_mov_b32_e32 v98, v4
	v_mov_b32_e32 v99, v4
	v_mov_b32_e32 v104, v4
	v_mov_b32_e32 v105, v4
	v_mov_b32_e32 v106, v4
	v_mov_b32_e32 v107, v4
	v_mov_b32_e32 v112, v4
	v_mov_b32_e32 v113, v4
	v_mov_b32_e32 v114, v4
	v_mov_b32_e32 v115, v4
	v_mov_b32_e32 v120, v4
	v_mov_b32_e32 v121, v4
	v_mov_b32_e32 v122, v4
	v_mov_b32_e32 v123, v4
	v_mov_b32_e32 v76, v4
	v_mov_b32_e32 v77, v4
	v_mov_b32_e32 v78, v4
	v_mov_b32_e32 v79, v4
	v_mov_b32_e32 v84, v4
	v_mov_b32_e32 v85, v4
	v_mov_b32_e32 v86, v4
	v_mov_b32_e32 v87, v4
	v_mov_b32_e32 v92, v4
	v_mov_b32_e32 v93, v4
	v_mov_b32_e32 v94, v4
	v_mov_b32_e32 v95, v4
	v_mov_b32_e32 v100, v4
	v_mov_b32_e32 v101, v4
	v_mov_b32_e32 v102, v4
	v_mov_b32_e32 v103, v4
	v_mov_b32_e32 v108, v4
	v_mov_b32_e32 v109, v4
	v_mov_b32_e32 v110, v4
	v_mov_b32_e32 v111, v4
	v_mov_b32_e32 v116, v4
	v_mov_b32_e32 v117, v4
	v_mov_b32_e32 v118, v4
	v_mov_b32_e32 v119, v4
	v_mov_b32_e32 v124, v4
	v_mov_b32_e32 v125, v4
	v_mov_b32_e32 v126, v4
	v_mov_b32_e32 v127, v4
	v_mov_b32_e32 v128, v4
	v_mov_b32_e32 v129, v4
	v_mov_b32_e32 v130, v4
	v_mov_b32_e32 v131, v4
	.p2align 6

; #define PG8_STR(x) PG8_STR2(x)
;     __device__ __forceinline__ bool next(int i, Unit& u) const { const int L = i * G + c; if (L >= 32) return false; u.pm = L; u.pn = L >> 4; return true; }
;     __device__ __forceinline__ bool next(int i, Unit& u) const { if (i != 0) return false; u.pm = pm; u.pn = pn; return true; }
;     __device__ __forceinline__ bool next(int i, Unit& u) const { if (i > 3) return false; u.pm = (i >> 1) * 16 + 2 * x + (i & 1); u.pn = i >> 1; return true; }
; template <class Epi, class Sched, bool ALIGN_EPI = false, bool SP2 = false>
; __device__ __forceinline__ void gemm_phase(PG8_LAS unsigned char* lds, const Gemm g, const Sched& S, const Epi& E) {
;     ...
;         const bool has_next = S.next(ui + 1, nxt);
;         const char* nA = has_next ? (const char*)g.A + (size_t)nxt.pm * tstepA : cA; const char* nB = has_next ? (const char*)g.Bt + (size_t)nxt.pn * tstepB : cB;
;         for (int t = 0; t < nt; t += 2) {
;     ...
;             asm volatile(".p2align 6\n\t.rept " PG8_STR(KLOOP_ALIGN) "\n\ts_nop 0\n\t.endr");
;     ...
;             const bool last = (t == nt - 2);
;             const char* a1 = cA + (size_t)(t + 1) * kstep;
;             const char* a2 = last ? nA : cA + (size_t)(t + 2) * kstep; const char* b2 = last ? nB : cB + (size_t)(t + 2) * kstep;
;             const char* a3 = a2 + kstep; const char* b3 = b2 + kstep;
;     ...
; #pragma unroll
;         for (int a = 0; a < 2; ++a)
; #pragma unroll
;             for (int b = 0; b < 2; ++b)
; #pragma unroll
;                 for (int m = 0; m < 4; ++m)
; #pragma unroll
;                     for (int n = 0; n < 2; ++n) acc[a][b][m][n] = (f32x4){0.f, 0.f, 0.f, 0.f};
.LBB0_1092:
	s_ashr_i32 s15, s14, 31
	s_lshl_b64 s[18:19], s[14:15], 19
	s_add_u32 s18, s29, s18
	s_addc_u32 s19, s30, s19
	s_and_b64 s[20:21], s[4:5], exec
	s_cselect_b32 s15, s19, s25
	s_cselect_b32 s44, s18, s24
	s_ashr_i32 s13, s12, 31
	s_lshl_b64 s[20:21], s[12:13], 19
	s_add_u32 s20, s31, s20
	s_addc_u32 s21, s33, s21
	s_and_b64 s[26:27], s[4:5], exec
	s_cselect_b32 s13, s21, s23
	s_cselect_b32 s45, s20, s22
	s_add_u32 s46, s22, 0x100
	s_addc_u32 s47, s23, 0
	s_add_u32 s22, s24, 0x40080
	v_mov_b32_e32 v4, 0
	s_addc_u32 s23, s25, 0
	s_mov_b32 s48, -2
	v_mov_b32_e32 v5, v4
	v_mov_b32_e32 v6, v4
	v_mov_b32_e32 v7, v4
	v_mov_b32_e32 v8, v4
	v_mov_b32_e32 v9, v4
	v_mov_b32_e32 v10, v4
	v_mov_b32_e32 v11, v4
	v_mov_b32_e32 v12, v4
	v_mov_b32_e32 v13, v4
	v_mov_b32_e32 v14, v4
	v_mov_b32_e32 v15, v4
	v_mov_b32_e32 v20, v4
	v_mov_b32_e32 v21, v4
	v_mov_b32_e32 v22, v4
	v_mov_b32_e32 v23, v4
	v_mov_b32_e32 v28, v4
	v_mov_b32_e32 v29, v4
	v_mov_b32_e32 v30, v4
	v_mov_b32_e32 v31, v4
	v_mov_b32_e32 v36, v4
	v_mov_b32_e32 v37, v4
	v_mov_b32_e32 v38, v4
	v_mov_b32_e32 v39, v4
	v_mov_b32_e32 v44, v4
	v_mov_b32_e32 v45, v4
	v_mov_b32_e32 v46, v4
	v_mov_b32_e32 v47, v4
	v_mov_b32_e32 v52, v4
	v_mov_b32_e32 v53, v4
	v_mov_b32_e32 v54, v4
	v_mov_b32_e32 v55, v4
	v_mov_b32_e32 v16, v4
	v_mov_b32_e32 v17, v4
	v_mov_b32_e32 v18, v4
	v_mov_b32_e32 v19, v4
	v_mov_b32_e32 v24, v4
	v_mov_b32_e32 v25, v4
	v_mov_b32_e32 v26, v4
	v_mov_b32_e32 v27, v4
	v_mov_b32_e32 v32, v4
	v_mov_b32_e32 v33, v4
	v_mov_b32_e32 v34, v4
	v_mov_b32_e32 v35, v4
	v_mov_b32_e32 v40, v4
	v_mov_b32_e32 v41, v4
	v_mov_b32_e32 v42, v4
	v_mov_b32_e32 v43, v4
	v_mov_b32_e32 v48, v4
	v_mov_b32_e32 v49, v4
	v_mov_b32_e32 v50, v4
	v_mov_b32_e32 v51, v4
	v_mov_b32_e32 v56, v4
	v_mov_b32_e32 v57, v4
	v_mov_b32_e32 v58, v4
	v_mov_b32_e32 v59, v4
	v_mov_b32_e32 v60, v4
	v_mov_b32_e32 v61, v4
	v_mov_b32_e32 v62, v4
	v_mov_b32_e32 v63, v4
	v_mov_b32_e32 v64, v4
	v_mov_b32_e32 v65, v4
	v_mov_b32_e32 v66, v4
	v_mov_b32_e32 v67, v4
	v_mov_b32_e32 v68, v4
	v_mov_b32_e32 v69, v4
	v_mov_b32_e32 v70, v4
	v_mov_b32_e32 v71, v4
	v_mov_b32_e32 v72, v4
	v_mov_b32_e32 v73, v4
	v_mov_b32_e32 v74, v4
	v_mov_b32_e32 v75, v4
	v_mov_b32_e32 v76, v4
	v_mov_b32_e32 v77, v4
	v_mov_b32_e32 v78, v4
	v_mov_b32_e32 v79, v4
	v_mov_b32_e32 v84, v4
	v_mov_b32_e32 v85, v4
	v_mov_b32_e32 v86, v4
	v_mov_b32_e32 v87, v4
	v_mov_b32_e32 v92, v4
	v_mov_b32_e32 v93, v4
	v_mov_b32_e32 v94, v4
	v_mov_b32_e32 v95, v4
	v_mov_b32_e32 v100, v4
	v_mov_b32_e32 v101, v4
	v_mov_b32_e32 v102, v4
	v_mov_b32_e32 v103, v4
	v_mov_b32_e32 v108, v4
	v_mov_b32_e32 v109, v4
	v_mov_b32_e32 v110, v4
	v_mov_b32_e32 v111, v4
	v_mov_b32_e32 v116, v4
	v_mov_b32_e32 v117, v4
	v_mov_b32_e32 v118, v4
	v_mov_b32_e32 v119, v4
	v_mov_b32_e32 v80, v4
	v_mov_b32_e32 v81, v4
	v_mov_b32_e32 v82, v4
	v_mov_b32_e32 v83, v4
	v_mov_b32_e32 v88, v4
	v_mov_b32_e32 v89, v4
	v_mov_b32_e32 v90, v4
	v_mov_b32_e32 v91, v4
	v_mov_b32_e32 v96, v4
	v_mov_b32_e32 v97, v4
	v_mov_b32_e32 v98, v4
	v_mov_b32_e32 v99, v4
	v_mov_b32_e32 v104, v4
	v_mov_b32_e32 v105, v4
	v_mov_b32_e32 v106, v4
	v_mov_b32_e32 v107, v4
	v_mov_b32_e32 v112, v4
	v_mov_b32_e32 v113, v4
	v_mov_b32_e32 v114, v4
	v_mov_b32_e32 v115, v4
	v_mov_b32_e32 v120, v4
	v_mov_b32_e32 v121, v4
	v_mov_b32_e32 v122, v4
	v_mov_b32_e32 v123, v4
	v_mov_b32_e32 v124, v4
	v_mov_b32_e32 v125, v4
	v_mov_b32_e32 v126, v4
	v_mov_b32_e32 v127, v4
	v_mov_b32_e32 v128, v4
	v_mov_b32_e32 v129, v4
	v_mov_b32_e32 v130, v4
	v_mov_b32_e32 v131, v4
	.p2align 6

; #define PG8_STR(x) PG8_STR2(x)
;     __device__ __forceinline__ bool next(int i, Unit& u) const { const int L = i * G + c; if (L >= 32) return false; u.pm = L; u.pn = L >> 4; return true; }
;     __device__ __forceinline__ bool next(int i, Unit& u) const { if (i != 0) return false; u.pm = pm; u.pn = pn; return true; }
;     __device__ __forceinline__ bool next(int i, Unit& u) const { if (i > 3) return false; u.pm = (i >> 1) * 16 + 2 * x + (i & 1); u.pn = i >> 1; return true; }
; template <class Epi, class Sched, bool ALIGN_EPI = false, bool SP2 = false>
; __device__ __forceinline__ void gemm_phase(PG8_LAS unsigned char* lds, const Gemm g, const Sched& S, const Epi& E) {
;     ...
;         const bool has_next = S.next(ui + 1, nxt);
;         const char* nA = has_next ? (const char*)g.A + (size_t)nxt.pm * tstepA : cA; const char* nB = has_next ? (const char*)g.Bt + (size_t)nxt.pn * tstepB : cB;
;         for (int t = 0; t < nt; t += 2) {
;     ...
;             asm volatile(".p2align 6\n\t.rept " PG8_STR(KLOOP_ALIGN) "\n\ts_nop 0\n\t.endr");
;     ...
;             const bool last = (t == nt - 2);
;             const char* a1 = cA + (size_t)(t + 1) * kstep;
;             const char* a2 = last ? nA : cA + (size_t)(t + 2) * kstep; const char* b2 = last ? nB : cB + (size_t)(t + 2) * kstep;
;             const char* a3 = a2 + kstep; const char* b3 = b2 + kstep;
;     ...
; #pragma unroll
;         for (int a = 0; a < 2; ++a)
; #pragma unroll
;             for (int b = 0; b < 2; ++b)
; #pragma unroll
;                 for (int m = 0; m < 4; ++m)
; #pragma unroll
;                     for (int n = 0; n < 2; ++n) acc[a][b][m][n] = (f32x4){0.f, 0.f, 0.f, 0.f};
.LBB0_1160:
	s_mov_b64 s[24:25], s[4:5]
	s_and_b64 s[4:5], s[16:17], exec
	s_mov_b64 s[22:23], s[6:7]
	s_cselect_b32 s6, s42, s42
	s_cselect_b32 s4, s43, s43
	s_ashr_i32 s7, s6, 31
	s_lshl_b64 s[6:7], s[6:7], 19
	s_add_u32 s6, s0, s6
	s_addc_u32 s7, s1, s7
	s_and_b64 s[26:27], s[16:17], exec
	s_cselect_b32 s19, s7, s23
	s_cselect_b32 s21, s6, s22
	s_ashr_i32 s5, s4, 31
	s_lshl_b64 s[4:5], s[4:5], 19
	s_add_u32 s4, s28, s4
	s_addc_u32 s5, s29, s5
	s_and_b64 s[26:27], s[16:17], exec
	s_cselect_b32 s44, s5, s25
	s_cselect_b32 s45, s4, s24
	s_add_u32 s46, s24, 0x100
	s_addc_u32 s47, s25, 0
	s_add_u32 s22, s22, 0x40080
	v_mov_b32_e32 v4, 0
	s_addc_u32 s23, s23, 0
	s_mov_b32 s48, -2
	v_mov_b32_e32 v5, v4
	v_mov_b32_e32 v6, v4
	v_mov_b32_e32 v7, v4
	v_mov_b32_e32 v8, v4
	v_mov_b32_e32 v9, v4
	v_mov_b32_e32 v10, v4
	v_mov_b32_e32 v11, v4
	v_mov_b32_e32 v16, v4
	v_mov_b32_e32 v17, v4
	v_mov_b32_e32 v18, v4
	v_mov_b32_e32 v19, v4
	v_mov_b32_e32 v24, v4
	v_mov_b32_e32 v25, v4
	v_mov_b32_e32 v26, v4
	v_mov_b32_e32 v27, v4
	v_mov_b32_e32 v32, v4
	v_mov_b32_e32 v33, v4
	v_mov_b32_e32 v34, v4
	v_mov_b32_e32 v35, v4
	v_mov_b32_e32 v40, v4
	v_mov_b32_e32 v41, v4
	v_mov_b32_e32 v42, v4
	v_mov_b32_e32 v43, v4
	v_mov_b32_e32 v48, v4
	v_mov_b32_e32 v49, v4
	v_mov_b32_e32 v50, v4
	v_mov_b32_e32 v51, v4
	v_mov_b32_e32 v56, v4
	v_mov_b32_e32 v57, v4
	v_mov_b32_e32 v58, v4
	v_mov_b32_e32 v59, v4
	v_mov_b32_e32 v12, v4
	v_mov_b32_e32 v13, v4
	v_mov_b32_e32 v14, v4
	v_mov_b32_e32 v15, v4
	v_mov_b32_e32 v20, v4
	v_mov_b32_e32 v21, v4
	v_mov_b32_e32 v22, v4
	v_mov_b32_e32 v23, v4
	v_mov_b32_e32 v28, v4
	v_mov_b32_e32 v29, v4
	v_mov_b32_e32 v30, v4
	v_mov_b32_e32 v31, v4
	v_mov_b32_e32 v36, v4
	v_mov_b32_e32 v37, v4
	v_mov_b32_e32 v38, v4
	v_mov_b32_e32 v39, v4
	v_mov_b32_e32 v44, v4
	v_mov_b32_e32 v45, v4
	v_mov_b32_e32 v46, v4
	v_mov_b32_e32 v47, v4
	v_mov_b32_e32 v52, v4
	v_mov_b32_e32 v53, v4
	v_mov_b32_e32 v54, v4
	v_mov_b32_e32 v55, v4
	v_mov_b32_e32 v60, v4
	v_mov_b32_e32 v61, v4
	v_mov_b32_e32 v62, v4
	v_mov_b32_e32 v63, v4
	v_mov_b32_e32 v64, v4
	v_mov_b32_e32 v65, v4
	v_mov_b32_e32 v66, v4
	v_mov_b32_e32 v67, v4
	v_mov_b32_e32 v68, v4
	v_mov_b32_e32 v69, v4
	v_mov_b32_e32 v70, v4
	v_mov_b32_e32 v71, v4
	v_mov_b32_e32 v72, v4
	v_mov_b32_e32 v73, v4
	v_mov_b32_e32 v74, v4
	v_mov_b32_e32 v75, v4
	v_mov_b32_e32 v84, v4
	v_mov_b32_e32 v85, v4
	v_mov_b32_e32 v86, v4
	v_mov_b32_e32 v87, v4
	v_mov_b32_e32 v88, v4
	v_mov_b32_e32 v89, v4
	v_mov_b32_e32 v90, v4
	v_mov_b32_e32 v91, v4
	v_mov_b32_e32 v100, v4
	v_mov_b32_e32 v101, v4
	v_mov_b32_e32 v102, v4
	v_mov_b32_e32 v103, v4
	v_mov_b32_e32 v104, v4
	v_mov_b32_e32 v105, v4
	v_mov_b32_e32 v106, v4
	v_mov_b32_e32 v107, v4
	v_mov_b32_e32 v116, v4
	v_mov_b32_e32 v117, v4
	v_mov_b32_e32 v118, v4
	v_mov_b32_e32 v119, v4
	v_mov_b32_e32 v120, v4
	v_mov_b32_e32 v121, v4
	v_mov_b32_e32 v122, v4
	v_mov_b32_e32 v123, v4
	v_mov_b32_e32 v76, v4
	v_mov_b32_e32 v77, v4
	v_mov_b32_e32 v78, v4
	v_mov_b32_e32 v79, v4
	v_mov_b32_e32 v80, v4
	v_mov_b32_e32 v81, v4
	v_mov_b32_e32 v82, v4
	v_mov_b32_e32 v83, v4
	v_mov_b32_e32 v92, v4
	v_mov_b32_e32 v93, v4
	v_mov_b32_e32 v94, v4
	v_mov_b32_e32 v95, v4
	v_mov_b32_e32 v96, v4
	v_mov_b32_e32 v97, v4
	v_mov_b32_e32 v98, v4
	v_mov_b32_e32 v99, v4
	v_mov_b32_e32 v108, v4
	v_mov_b32_e32 v109, v4
	v_mov_b32_e32 v110, v4
	v_mov_b32_e32 v111, v4
	v_mov_b32_e32 v112, v4
	v_mov_b32_e32 v113, v4
	v_mov_b32_e32 v114, v4
	v_mov_b32_e32 v115, v4
	v_mov_b32_e32 v124, v4
	v_mov_b32_e32 v125, v4
	v_mov_b32_e32 v126, v4
	v_mov_b32_e32 v127, v4
	v_mov_b32_e32 v128, v4
	v_mov_b32_e32 v129, v4
	v_mov_b32_e32 v130, v4
	v_mov_b32_e32 v131, v4
	.p2align 6

;     __device__ __forceinline__ bool next(int i, Unit& u) const { const int L = i * G + c; if (L >= 32) return false; u.pm = L; u.pn = L >> 4; return true; }
;     __device__ __forceinline__ bool next(int i, Unit& u) const { if (i != 0) return false; u.pm = pm; u.pn = pn; return true; }
; template <class Epi, class Sched, bool ALIGN_EPI = false, bool SP2 = false>
; __device__ __forceinline__ void gemm_phase(PG8_LAS unsigned char* lds, const Gemm g, const Sched& S, const Epi& E) {
;     ...
; #pragma unroll
;         for (int a = 0; a < 2; ++a)
; #pragma unroll
;             for (int b = 0; b < 2; ++b)
; #pragma unroll
;                 for (int m = 0; m < 4; ++m)
; #pragma unroll
;                     for (int n = 0; n < 2; ++n) acc[a][b][m][n] = (f32x4){0.f, 0.f, 0.f, 0.f};
;     __device__ __forceinline__ bool next(int i, Unit& u) const { if (i > 3) return false; u.pm = (i >> 1) * 16 + 2 * x + (i & 1); u.pn = i >> 1; return true; }
.LBB0_1234:
	s_add_i32 s40, s41, 1
	s_mov_b32 s14, s38
	s_lshr_b32 s38, s40, 1
	s_lshl_b32 s12, s38, 4
	s_and_b32 s13, s40, 1
	s_or_b32 s12, s12, s13
	s_mov_b32 s15, s39
	s_or_b32 s39, s12, s27
	s_cmp_lt_u32 s41, 3
	s_cselect_b64 s[20:21], -1, 0
	s_and_b64 s[12:13], s[20:21], exec
	s_cselect_b32 s12, s39, s15
	s_cselect_b32 s14, s38, s14
	s_ashr_i32 s13, s12, 31
	s_lshl_b64 s[12:13], s[12:13], 19
	s_add_u32 s12, s24, s12
	s_addc_u32 s13, s25, s13
	s_ashr_i32 s15, s14, 31
	s_lshl_b64 s[14:15], s[14:15], 20
	s_add_u32 s14, s4, s14
	v_mov_b32_e32 v127, 0
	s_addc_u32 s15, s5, s15
	s_andn2_b64 vcc, exec, s[8:9]
	v_mov_b32_e32 v126, v127
	v_mov_b32_e32 v125, v127
	v_mov_b32_e32 v124, v127
	v_mov_b32_e32 v131, v127
	v_mov_b32_e32 v130, v127
	v_mov_b32_e32 v129, v127
	v_mov_b32_e32 v128, v127
	v_mov_b32_e32 v115, v127
	v_mov_b32_e32 v114, v127
	v_mov_b32_e32 v113, v127
	v_mov_b32_e32 v112, v127
	v_mov_b32_e32 v111, v127
	v_mov_b32_e32 v110, v127
	v_mov_b32_e32 v109, v127
	v_mov_b32_e32 v108, v127
	v_mov_b32_e32 v99, v127
	v_mov_b32_e32 v98, v127
	v_mov_b32_e32 v97, v127
	v_mov_b32_e32 v96, v127
	v_mov_b32_e32 v95, v127
	v_mov_b32_e32 v94, v127
	v_mov_b32_e32 v93, v127
	v_mov_b32_e32 v92, v127
	v_mov_b32_e32 v83, v127
	v_mov_b32_e32 v82, v127
	v_mov_b32_e32 v81, v127
	v_mov_b32_e32 v80, v127
	v_mov_b32_e32 v79, v127
	v_mov_b32_e32 v78, v127
	v_mov_b32_e32 v77, v127
	v_mov_b32_e32 v76, v127
	v_mov_b32_e32 v123, v127
	v_mov_b32_e32 v122, v127
	v_mov_b32_e32 v121, v127
	v_mov_b32_e32 v120, v127
	v_mov_b32_e32 v119, v127
	v_mov_b32_e32 v118, v127
	v_mov_b32_e32 v117, v127
	v_mov_b32_e32 v116, v127
	v_mov_b32_e32 v107, v127
	v_mov_b32_e32 v106, v127
	v_mov_b32_e32 v105, v127
	v_mov_b32_e32 v104, v127
	v_mov_b32_e32 v103, v127
	v_mov_b32_e32 v102, v127
	v_mov_b32_e32 v101, v127
	v_mov_b32_e32 v100, v127
	v_mov_b32_e32 v91, v127
	v_mov_b32_e32 v90, v127
	v_mov_b32_e32 v89, v127
	v_mov_b32_e32 v88, v127
	v_mov_b32_e32 v87, v127
	v_mov_b32_e32 v86, v127
	v_mov_b32_e32 v85, v127
	v_mov_b32_e32 v84, v127
	v_mov_b32_e32 v75, v127
	v_mov_b32_e32 v74, v127
	v_mov_b32_e32 v73, v127
	v_mov_b32_e32 v72, v127
	v_mov_b32_e32 v71, v127
	v_mov_b32_e32 v70, v127
	v_mov_b32_e32 v69, v127
	v_mov_b32_e32 v68, v127
	v_mov_b32_e32 v67, v127
	v_mov_b32_e32 v66, v127
	v_mov_b32_e32 v65, v127
	v_mov_b32_e32 v64, v127
	v_mov_b32_e32 v63, v127
	v_mov_b32_e32 v62, v127
	v_mov_b32_e32 v61, v127
	v_mov_b32_e32 v60, v127
	v_mov_b32_e32 v51, v127
	v_mov_b32_e32 v50, v127
	v_mov_b32_e32 v49, v127
	v_mov_b32_e32 v48, v127
	v_mov_b32_e32 v47, v127
	v_mov_b32_e32 v46, v127
	v_mov_b32_e32 v45, v127
	v_mov_b32_e32 v44, v127
	v_mov_b32_e32 v35, v127
	v_mov_b32_e32 v34, v127
	v_mov_b32_e32 v33, v127
	v_mov_b32_e32 v32, v127
	v_mov_b32_e32 v31, v127
	v_mov_b32_e32 v30, v127
	v_mov_b32_e32 v29, v127
	v_mov_b32_e32 v28, v127
	v_mov_b32_e32 v19, v127
	v_mov_b32_e32 v18, v127
	v_mov_b32_e32 v17, v127
	v_mov_b32_e32 v16, v127
	v_mov_b32_e32 v15, v127
	v_mov_b32_e32 v14, v127
	v_mov_b32_e32 v13, v127
	v_mov_b32_e32 v12, v127
	v_mov_b32_e32 v59, v127
	v_mov_b32_e32 v58, v127
	v_mov_b32_e32 v57, v127
	v_mov_b32_e32 v56, v127
	v_mov_b32_e32 v55, v127
	v_mov_b32_e32 v54, v127
	v_mov_b32_e32 v53, v127
	v_mov_b32_e32 v52, v127
	v_mov_b32_e32 v43, v127
	v_mov_b32_e32 v42, v127
	v_mov_b32_e32 v41, v127
	v_mov_b32_e32 v40, v127
	v_mov_b32_e32 v39, v127
	v_mov_b32_e32 v38, v127
	v_mov_b32_e32 v37, v127
	v_mov_b32_e32 v36, v127
	v_mov_b32_e32 v27, v127
	v_mov_b32_e32 v26, v127
	v_mov_b32_e32 v25, v127
	v_mov_b32_e32 v24, v127
	v_mov_b32_e32 v23, v127
	v_mov_b32_e32 v22, v127
	v_mov_b32_e32 v21, v127
	v_mov_b32_e32 v20, v127
	v_mov_b32_e32 v11, v127
	v_mov_b32_e32 v10, v127
	v_mov_b32_e32 v9, v127
	v_mov_b32_e32 v8, v127
	v_mov_b32_e32 v7, v127
	v_mov_b32_e32 v6, v127
	v_mov_b32_e32 v5, v127
	v_mov_b32_e32 v4, v127
	s_cbranch_vccnz .LBB0_1237
; #define PG8_STR(x) PG8_STR2(x)
; template <class Epi, class Sched, bool ALIGN_EPI = false, bool SP2 = false>
; __device__ __forceinline__ void gemm_phase(PG8_LAS unsigned char* lds, const Gemm g, const Sched& S, const Epi& E) {
;     ...
;         const char* nA = has_next ? (const char*)g.A + (size_t)nxt.pm * tstepA : cA; const char* nB = has_next ? (const char*)g.Bt + (size_t)nxt.pn * tstepB : cB;
;         for (int t = 0; t < nt; t += 2) {
;     ...
;             asm volatile(".p2align 6\n\t.rept " PG8_STR(KLOOP_ALIGN) "\n\ts_nop 0\n\t.endr");
;     ...
;             const bool last = (t == nt - 2);
;             const char* a1 = cA + (size_t)(t + 1) * kstep;
;             const char* a2 = last ? nA : cA + (size_t)(t + 2) * kstep; const char* b2 = last ? nB : cB + (size_t)(t + 2) * kstep;
;             const char* a3 = a2 + kstep; const char* b3 = b2 + kstep;
;     ...
; #pragma unroll
;         for (int a = 0; a < 2; ++a)
; #pragma unroll
;             for (int b = 0; b < 2; ++b)
; #pragma unroll
;                 for (int m = 0; m < 4; ++m)
; #pragma unroll
;                     for (int n = 0; n < 2; ++n) acc[a][b][m][n] = (f32x4){0.f, 0.f, 0.f, 0.f};
	s_and_b64 s[20:21], s[20:21], exec
	s_cselect_b32 s43, s13, s17
	s_cselect_b32 s44, s12, s16
	s_cselect_b32 s45, s15, s19
	s_cselect_b32 s46, s14, s18
	s_add_u32 s47, s18, 0x100
	s_addc_u32 s48, s19, 0
	s_add_u32 s16, s16, 0x40080
	v_mov_b32_e32 v4, 0
	s_addc_u32 s17, s17, 0
	s_mov_b32 s18, 0
	v_mov_b32_e32 v5, v4
	v_mov_b32_e32 v6, v4
	v_mov_b32_e32 v7, v4
	v_mov_b32_e32 v8, v4
	v_mov_b32_e32 v9, v4
	v_mov_b32_e32 v10, v4
	v_mov_b32_e32 v11, v4
	v_mov_b32_e32 v20, v4
	v_mov_b32_e32 v21, v4
	v_mov_b32_e32 v22, v4
	v_mov_b32_e32 v23, v4
	v_mov_b32_e32 v24, v4
	v_mov_b32_e32 v25, v4
	v_mov_b32_e32 v26, v4
	v_mov_b32_e32 v27, v4
	v_mov_b32_e32 v36, v4
	v_mov_b32_e32 v37, v4
	v_mov_b32_e32 v38, v4
	v_mov_b32_e32 v39, v4
	v_mov_b32_e32 v40, v4
	v_mov_b32_e32 v41, v4
	v_mov_b32_e32 v42, v4
	v_mov_b32_e32 v43, v4
	v_mov_b32_e32 v52, v4
	v_mov_b32_e32 v53, v4
	v_mov_b32_e32 v54, v4
	v_mov_b32_e32 v55, v4
	v_mov_b32_e32 v56, v4
	v_mov_b32_e32 v57, v4
	v_mov_b32_e32 v58, v4
	v_mov_b32_e32 v59, v4
	v_mov_b32_e32 v12, v4
	v_mov_b32_e32 v13, v4
	v_mov_b32_e32 v14, v4
	v_mov_b32_e32 v15, v4
	v_mov_b32_e32 v16, v4
	v_mov_b32_e32 v17, v4
	v_mov_b32_e32 v18, v4
	v_mov_b32_e32 v19, v4
	v_mov_b32_e32 v28, v4
	v_mov_b32_e32 v29, v4
	v_mov_b32_e32 v30, v4
	v_mov_b32_e32 v31, v4
	v_mov_b32_e32 v32, v4
	v_mov_b32_e32 v33, v4
	v_mov_b32_e32 v34, v4
	v_mov_b32_e32 v35, v4
	v_mov_b32_e32 v44, v4
	v_mov_b32_e32 v45, v4
	v_mov_b32_e32 v46, v4
	v_mov_b32_e32 v47, v4
	v_mov_b32_e32 v48, v4
	v_mov_b32_e32 v49, v4
	v_mov_b32_e32 v50, v4
	v_mov_b32_e32 v51, v4
	v_mov_b32_e32 v60, v4
	v_mov_b32_e32 v61, v4
	v_mov_b32_e32 v62, v4
	v_mov_b32_e32 v63, v4
	v_mov_b32_e32 v64, v4
	v_mov_b32_e32 v65, v4
	v_mov_b32_e32 v66, v4
	v_mov_b32_e32 v67, v4
	v_mov_b32_e32 v68, v4
	v_mov_b32_e32 v69, v4
	v_mov_b32_e32 v70, v4
	v_mov_b32_e32 v71, v4
	v_mov_b32_e32 v72, v4
	v_mov_b32_e32 v73, v4
	v_mov_b32_e32 v74, v4
	v_mov_b32_e32 v75, v4
	v_mov_b32_e32 v84, v4
	v_mov_b32_e32 v85, v4
	v_mov_b32_e32 v86, v4
	v_mov_b32_e32 v87, v4
	v_mov_b32_e32 v88, v4
	v_mov_b32_e32 v89, v4
	v_mov_b32_e32 v90, v4
	v_mov_b32_e32 v91, v4
	v_mov_b32_e32 v100, v4
	v_mov_b32_e32 v101, v4
	v_mov_b32_e32 v102, v4
	v_mov_b32_e32 v103, v4
	v_mov_b32_e32 v104, v4
	v_mov_b32_e32 v105, v4
	v_mov_b32_e32 v106, v4
	v_mov_b32_e32 v107, v4
	v_mov_b32_e32 v116, v4
	v_mov_b32_e32 v117, v4
	v_mov_b32_e32 v118, v4
	v_mov_b32_e32 v119, v4
	v_mov_b32_e32 v120, v4
	v_mov_b32_e32 v121, v4
	v_mov_b32_e32 v122, v4
	v_mov_b32_e32 v123, v4
	v_mov_b32_e32 v76, v4
	v_mov_b32_e32 v77, v4
	v_mov_b32_e32 v78, v4
	v_mov_b32_e32 v79, v4
	v_mov_b32_e32 v80, v4
	v_mov_b32_e32 v81, v4
	v_mov_b32_e32 v82, v4
	v_mov_b32_e32 v83, v4
	v_mov_b32_e32 v92, v4
	v_mov_b32_e32 v93, v4
	v_mov_b32_e32 v94, v4
	v_mov_b32_e32 v95, v4
	v_mov_b32_e32 v96, v4
	v_mov_b32_e32 v97, v4
	v_mov_b32_e32 v98, v4
	v_mov_b32_e32 v99, v4
	v_mov_b32_e32 v108, v4
	v_mov_b32_e32 v109, v4
	v_mov_b32_e32 v110, v4
	v_mov_b32_e32 v111, v4
	v_mov_b32_e32 v112, v4
	v_mov_b32_e32 v113, v4
	v_mov_b32_e32 v114, v4
	v_mov_b32_e32 v115, v4
	v_mov_b32_e32 v128, v4
	v_mov_b32_e32 v129, v4
	v_mov_b32_e32 v130, v4
	v_mov_b32_e32 v131, v4
	v_mov_b32_e32 v124, v4
	v_mov_b32_e32 v125, v4
	v_mov_b32_e32 v126, v4
	v_mov_b32_e32 v127, v4
	.p2align 6

; #define PG8_STAGE(bufoff, gbase, voff) do { _Pragma("unroll") for (int _i = 0; _i < 2; ++_i) \
;         __builtin_amdgcn_global_load_lds((const unsigned*)((const char*)(gbase) + (voff)[_i]), (PG8_LAS unsigned*)(lds + (bufoff) + ldsw + _i * 8192), 16, 0, 0); } while (0)
; #define PG8_WAIT_V(n) asm volatile("s_waitcnt vmcnt(" #n ")" ::: "memory")
; #define PG8_BAR __builtin_amdgcn_s_barrier()
; template <class Epi, class Sched, bool ALIGN_EPI = false, bool SP2 = false>
; __device__ __forceinline__ void gemm_phase(PG8_LAS unsigned char* lds, const Gemm g, const Sched& S, const Epi& E) {
;     ...
;     f32x4 acc[2][2][4][2];
; #pragma unroll
;     for (int a = 0; a < 2; ++a)
; #pragma unroll
;         for (int b = 0; b < 2; ++b)
; #pragma unroll
;             for (int m = 0; m < 4; ++m)
; #pragma unroll
;                 for (int n = 0; n < 2; ++n) acc[a][b][m][n] = (f32x4){0.f, 0.f, 0.f, 0.f};
;     ...
;         PG8_STAGE(PG8_SB(0, 0), cB, voffB); PG8_STAGE(PG8_SB(0, 1), cB + hstepB, voffB); PG8_STAGE(PG8_SA(0, 0), cA, voffA); PG8_STAGE(PG8_SA(0, 1), cA + hstepA, voffA);
;         if (wr == 1) PG8_BAR;
;         PG8_WAIT_V(2); PG8_BAR;
;         PG8_STAGE(PG8_SB(1, 0), cB + kstep, voffB); PG8_STAGE(PG8_SA(1, 0), cA + kstep, voffA); PG8_STAGE(PG8_SB(1, 1), cB + hstepB + kstep, voffB);
;         PG8_WAIT_V(6); PG8_BAR;
.LBB0_1246:
	v_lshrrev_b32_e32 v15, 1, v14
	v_and_b32_e32 v144, 24, v15
	v_and_b32_e32 v2, 15, v14
	v_lshlrev_b32_e32 v15, 1, v144
	v_lshlrev_b32_e32 v14, 2, v14
	s_and_b32 s15, s8, 3
	v_lshl_or_b32 v15, v2, 6, v15
	s_lshl_b32 s8, s13, 13
	v_and_b32_e32 v14, 32, v14
	v_readlane_b32 s28, v253, 55
	v_bitop3_b32 v16, v15, s8, v14 bitop3:0xde
	s_lshl_b32 s8, s15, 12
	v_readlane_b32 s29, v253, 56
	v_bitop3_b32 v145, v15, s8, v14 bitop3:0xde
	s_lshr_b64 s[26:27], s[28:29], 2
	s_lshr_b32 s8, s29, 2
	s_lshl_b32 s25, s13, 6
	s_mul_i32 s8, s8, 0x580000
	s_mul_hi_u32 s13, s26, 0x580000
	s_add_i32 s13, s13, s8
	s_mul_i32 s8, s26, 0x580000
	s_add_u32 s26, s11, 0x8d00080
	v_mov_b32_e32 v135, v3
	s_addc_u32 s27, s12, 0
	v_mov_b32_e32 v139, v3
	s_add_i32 m0, s19, 0x18000
	v_lshl_add_u64 v[14:15], s[26:27], 0, v[134:135]
	s_waitcnt vmcnt(2)
	s_barrier
	global_load_lds_dwordx4 v[14:15], off
	v_lshl_add_u64 v[14:15], s[26:27], 0, v[138:139]
	s_add_i32 m0, s19, 0x1a000
	s_add_i32 s26, s19, 0x8000
	s_add_i32 s27, s19, 0xa000
	global_load_lds_dwordx4 v[14:15], off
	v_lshl_add_u64 v[6:7], v[6:7], 0, s[64:65]
	s_mov_b32 m0, s26
	s_add_u32 s28, s11, 0x8d40080
	global_load_lds_dwordx4 v[6:7], off
	v_lshl_add_u64 v[4:5], v[4:5], 0, s[64:65]
	s_mov_b32 m0, s27
	s_addc_u32 s29, s12, 0
	global_load_lds_dwordx4 v[4:5], off
	s_add_i32 m0, s19, 0x1c000
	v_lshl_add_u64 v[4:5], s[28:29], 0, v[134:135]
	global_load_lds_dwordx4 v[4:5], off
	v_lshl_add_u64 v[4:5], s[28:29], 0, v[138:139]
	s_add_i32 m0, s19, 0x1e000
	s_add_u32 s8, s8, s10
	global_load_lds_dwordx4 v[4:5], off
	s_addc_u32 s10, s13, 0
	s_add_u32 s8, s2, s8
	s_addc_u32 s10, s3, s10
	s_add_u32 s28, s8, 0x8d00100
	s_addc_u32 s29, s10, 0
	s_and_b32 s8, s23, 7
	s_lshl_b32 s8, s8, 22
	s_lshl_b32 s9, s9, 19
	v_lshlrev_b32_e32 v4, 14, v11
	s_or_b32 s8, s8, s9
	v_and_b32_e32 v4, 0xffff8000, v4
	s_add_u32 s23, s2, s8
	v_lshl_add_u32 v4, v12, 11, v4
	v_and_b32_e32 v5, 1, v11
	s_addc_u32 s30, s3, 0
	v_lshl_or_b32 v4, v5, 6, v4
	s_add_u32 s8, s23, 0xb040080
	v_lshl_add_u32 v4, v13, 1, v4
	v_mov_b32_e32 v5, v3
	s_addc_u32 s9, s30, 0
	v_lshl_add_u64 v[140:141], s[8:9], 0, v[4:5]
	v_lshlrev_b32_e32 v4, 14, v8
	v_and_b32_e32 v4, 0xffff8000, v4
	v_lshl_add_u32 v4, v9, 11, v4
	v_and_b32_e32 v5, 1, v8
	v_lshl_or_b32 v4, v5, 6, v4
	s_waitcnt vmcnt(6)
	v_lshl_add_u32 v4, v10, 1, v4
	v_mov_b32_e32 v5, v3
	v_lshl_add_u64 v[142:143], s[8:9], 0, v[4:5]
	v_mov_b32_e32 v4, 0
	s_mov_b32 s31, -2
	s_mov_b64 s[8:9], 0
	v_add_u32_e32 v146, 0, v16
	v_mov_b32_e32 v5, v4
	v_mov_b32_e32 v6, v4
	v_mov_b32_e32 v7, v4
	v_mov_b32_e32 v8, v4
	v_mov_b32_e32 v9, v4
	v_mov_b32_e32 v10, v4
	v_mov_b32_e32 v11, v4
	v_mov_b32_e32 v12, v4
	v_mov_b32_e32 v13, v4
	v_mov_b32_e32 v14, v4
	v_mov_b32_e32 v15, v4
	v_mov_b32_e32 v20, v4
	v_mov_b32_e32 v21, v4
	v_mov_b32_e32 v22, v4
	v_mov_b32_e32 v23, v4
	v_mov_b32_e32 v28, v4
	v_mov_b32_e32 v29, v4
	v_mov_b32_e32 v30, v4
	v_mov_b32_e32 v31, v4
	v_mov_b32_e32 v36, v4
	v_mov_b32_e32 v37, v4
	v_mov_b32_e32 v38, v4
	v_mov_b32_e32 v39, v4
	v_mov_b32_e32 v48, v4
	v_mov_b32_e32 v49, v4
	v_mov_b32_e32 v50, v4
	v_mov_b32_e32 v51, v4
	v_mov_b32_e32 v56, v4
	v_mov_b32_e32 v57, v4
	v_mov_b32_e32 v58, v4
	v_mov_b32_e32 v59, v4
	v_mov_b32_e32 v16, v4
	v_mov_b32_e32 v17, v4
	v_mov_b32_e32 v18, v4
	v_mov_b32_e32 v19, v4
	v_mov_b32_e32 v24, v4
	v_mov_b32_e32 v25, v4
	v_mov_b32_e32 v26, v4
	v_mov_b32_e32 v27, v4
	v_mov_b32_e32 v32, v4
	v_mov_b32_e32 v33, v4
	v_mov_b32_e32 v34, v4
	v_mov_b32_e32 v35, v4
	v_mov_b32_e32 v40, v4
	v_mov_b32_e32 v41, v4
	v_mov_b32_e32 v42, v4
	v_mov_b32_e32 v43, v4
	v_mov_b32_e32 v44, v4
	v_mov_b32_e32 v45, v4
	v_mov_b32_e32 v46, v4
	v_mov_b32_e32 v47, v4
	v_mov_b32_e32 v52, v4
	v_mov_b32_e32 v53, v4
	v_mov_b32_e32 v54, v4
	v_mov_b32_e32 v55, v4
	v_mov_b32_e32 v60, v4
	v_mov_b32_e32 v61, v4
	v_mov_b32_e32 v62, v4
	v_mov_b32_e32 v63, v4
	v_mov_b32_e32 v64, v4
	v_mov_b32_e32 v65, v4
	v_mov_b32_e32 v66, v4
	v_mov_b32_e32 v67, v4
	v_mov_b32_e32 v68, v4
	v_mov_b32_e32 v69, v4
	v_mov_b32_e32 v70, v4
	v_mov_b32_e32 v71, v4
	v_mov_b32_e32 v72, v4
	v_mov_b32_e32 v73, v4
	v_mov_b32_e32 v74, v4
	v_mov_b32_e32 v75, v4
	v_mov_b32_e32 v76, v4
	v_mov_b32_e32 v77, v4
	v_mov_b32_e32 v78, v4
	v_mov_b32_e32 v79, v4
	v_mov_b32_e32 v84, v4
	v_mov_b32_e32 v85, v4
	v_mov_b32_e32 v86, v4
	v_mov_b32_e32 v87, v4
	v_mov_b32_e32 v92, v4
	v_mov_b32_e32 v93, v4
	v_mov_b32_e32 v94, v4
	v_mov_b32_e32 v95, v4
	v_mov_b32_e32 v100, v4
	v_mov_b32_e32 v101, v4
	v_mov_b32_e32 v102, v4
	v_mov_b32_e32 v103, v4
	v_mov_b32_e32 v112, v4
	v_mov_b32_e32 v113, v4
	v_mov_b32_e32 v114, v4
	v_mov_b32_e32 v115, v4
	v_mov_b32_e32 v120, v4
	v_mov_b32_e32 v121, v4
	v_mov_b32_e32 v122, v4
	v_mov_b32_e32 v123, v4
	v_mov_b32_e32 v80, v4
	v_mov_b32_e32 v81, v4
	v_mov_b32_e32 v82, v4
	v_mov_b32_e32 v83, v4
	v_mov_b32_e32 v88, v4
	v_mov_b32_e32 v89, v4
	v_mov_b32_e32 v90, v4
	v_mov_b32_e32 v91, v4
	v_mov_b32_e32 v96, v4
	v_mov_b32_e32 v97, v4
	v_mov_b32_e32 v98, v4
	v_mov_b32_e32 v99, v4
	v_mov_b32_e32 v104, v4
	v_mov_b32_e32 v105, v4
	v_mov_b32_e32 v106, v4
	v_mov_b32_e32 v107, v4
	v_mov_b32_e32 v108, v4
	v_mov_b32_e32 v109, v4
	v_mov_b32_e32 v110, v4
	v_mov_b32_e32 v111, v4
	v_mov_b32_e32 v116, v4
	v_mov_b32_e32 v117, v4
	v_mov_b32_e32 v118, v4
	v_mov_b32_e32 v119, v4
	v_mov_b32_e32 v124, v4
	v_mov_b32_e32 v125, v4
	v_mov_b32_e32 v126, v4
	v_mov_b32_e32 v127, v4
	v_mov_b32_e32 v128, v4
	v_mov_b32_e32 v129, v4
	v_mov_b32_e32 v130, v4
	v_mov_b32_e32 v131, v4
	s_barrier
	.p2align 6

; #define PG8_STR(x) PG8_STR2(x)
;     __device__ __forceinline__ bool next(int i, Unit& u) const { const int L = i * G + c; if (L >= 32) return false; u.pm = L; u.pn = L >> 4; return true; }
;     __device__ __forceinline__ bool next(int i, Unit& u) const { if (i != 0) return false; u.pm = pm; u.pn = pn; return true; }
;     __device__ __forceinline__ bool next(int i, Unit& u) const { if (i > 3) return false; u.pm = (i >> 1) * 16 + 2 * x + (i & 1); u.pn = i >> 1; return true; }
; template <class Epi, class Sched, bool ALIGN_EPI = false, bool SP2 = false>
; __device__ __forceinline__ void gemm_phase(PG8_LAS unsigned char* lds, const Gemm g, const Sched& S, const Epi& E) {
;     ...
;         const bool has_next = S.next(ui + 1, nxt);
;         const char* nA = has_next ? (const char*)g.A + (size_t)nxt.pm * tstepA : cA; const char* nB = has_next ? (const char*)g.Bt + (size_t)nxt.pn * tstepB : cB;
;         for (int t = 0; t < nt; t += 2) {
;     ...
;             asm volatile(".p2align 6\n\t.rept " PG8_STR(KLOOP_ALIGN) "\n\ts_nop 0\n\t.endr");
;     ...
;             const bool last = (t == nt - 2);
;             const char* a1 = cA + (size_t)(t + 1) * kstep;
;             const char* a2 = last ? nA : cA + (size_t)(t + 2) * kstep; const char* b2 = last ? nB : cB + (size_t)(t + 2) * kstep;
;             const char* a3 = a2 + kstep; const char* b3 = b2 + kstep;
;     ...
; #pragma unroll
;         for (int a = 0; a < 2; ++a)
; #pragma unroll
;             for (int b = 0; b < 2; ++b)
; #pragma unroll
;                 for (int m = 0; m < 4; ++m)
; #pragma unroll
;                     for (int n = 0; n < 2; ++n) acc[a][b][m][n] = (f32x4){0.f, 0.f, 0.f, 0.f};
.LBB0_1692:
	s_ashr_i32 s13, s12, 31
	s_lshl_b64 s[16:17], s[12:13], 19
	s_add_u32 s16, s27, s16
	s_addc_u32 s17, s28, s17
	s_and_b64 s[18:19], s[2:3], exec
	s_cselect_b32 s13, s17, s23
	s_cselect_b32 s41, s16, s22
	s_ashr_i32 s11, s10, 31
	s_lshl_b64 s[18:19], s[10:11], 19
	s_add_u32 s18, s29, s18
	s_addc_u32 s19, s30, s19
	s_and_b64 s[24:25], s[2:3], exec
	s_cselect_b32 s11, s19, s21
	s_cselect_b32 s42, s18, s20
	s_add_u32 s43, s20, 0x100
	s_addc_u32 s44, s21, 0
	s_add_u32 s20, s22, 0x40080
	v_mov_b32_e32 v4, 0
	s_addc_u32 s21, s23, 0
	s_mov_b32 s45, -2
	v_mov_b32_e32 v5, v4
	v_mov_b32_e32 v6, v4
	v_mov_b32_e32 v7, v4
	v_mov_b32_e32 v8, v4
	v_mov_b32_e32 v9, v4
	v_mov_b32_e32 v10, v4
	v_mov_b32_e32 v11, v4
	v_mov_b32_e32 v12, v4
	v_mov_b32_e32 v13, v4
	v_mov_b32_e32 v14, v4
	v_mov_b32_e32 v15, v4
	v_mov_b32_e32 v20, v4
	v_mov_b32_e32 v21, v4
	v_mov_b32_e32 v22, v4
	v_mov_b32_e32 v23, v4
	v_mov_b32_e32 v28, v4
	v_mov_b32_e32 v29, v4
	v_mov_b32_e32 v30, v4
	v_mov_b32_e32 v31, v4
	v_mov_b32_e32 v36, v4
	v_mov_b32_e32 v37, v4
	v_mov_b32_e32 v38, v4
	v_mov_b32_e32 v39, v4
	v_mov_b32_e32 v44, v4
	v_mov_b32_e32 v45, v4
	v_mov_b32_e32 v46, v4
	v_mov_b32_e32 v47, v4
	v_mov_b32_e32 v52, v4
	v_mov_b32_e32 v53, v4
	v_mov_b32_e32 v54, v4
	v_mov_b32_e32 v55, v4
	v_mov_b32_e32 v16, v4
	v_mov_b32_e32 v17, v4
	v_mov_b32_e32 v18, v4
	v_mov_b32_e32 v19, v4
	v_mov_b32_e32 v24, v4
	v_mov_b32_e32 v25, v4
	v_mov_b32_e32 v26, v4
	v_mov_b32_e32 v27, v4
	v_mov_b32_e32 v32, v4
	v_mov_b32_e32 v33, v4
	v_mov_b32_e32 v34, v4
	v_mov_b32_e32 v35, v4
	v_mov_b32_e32 v40, v4
	v_mov_b32_e32 v41, v4
	v_mov_b32_e32 v42, v4
	v_mov_b32_e32 v43, v4
	v_mov_b32_e32 v48, v4
	v_mov_b32_e32 v49, v4
	v_mov_b32_e32 v50, v4
	v_mov_b32_e32 v51, v4
	v_mov_b32_e32 v56, v4
	v_mov_b32_e32 v57, v4
	v_mov_b32_e32 v58, v4
	v_mov_b32_e32 v59, v4
	v_mov_b32_e32 v60, v4
	v_mov_b32_e32 v61, v4
	v_mov_b32_e32 v62, v4
	v_mov_b32_e32 v63, v4
	v_mov_b32_e32 v64, v4
	v_mov_b32_e32 v65, v4
	v_mov_b32_e32 v66, v4
	v_mov_b32_e32 v67, v4
	v_mov_b32_e32 v68, v4
	v_mov_b32_e32 v69, v4
	v_mov_b32_e32 v70, v4
	v_mov_b32_e32 v71, v4
	v_mov_b32_e32 v72, v4
	v_mov_b32_e32 v73, v4
	v_mov_b32_e32 v74, v4
	v_mov_b32_e32 v75, v4
	v_mov_b32_e32 v76, v4
	v_mov_b32_e32 v77, v4
	v_mov_b32_e32 v78, v4
	v_mov_b32_e32 v79, v4
	v_mov_b32_e32 v84, v4
	v_mov_b32_e32 v85, v4
	v_mov_b32_e32 v86, v4
	v_mov_b32_e32 v87, v4
	v_mov_b32_e32 v92, v4
	v_mov_b32_e32 v93, v4
	v_mov_b32_e32 v94, v4
	v_mov_b32_e32 v95, v4
	v_mov_b32_e32 v100, v4
	v_mov_b32_e32 v101, v4
	v_mov_b32_e32 v102, v4
	v_mov_b32_e32 v103, v4
	v_mov_b32_e32 v108, v4
	v_mov_b32_e32 v109, v4
	v_mov_b32_e32 v110, v4
	v_mov_b32_e32 v111, v4
	v_mov_b32_e32 v116, v4
	v_mov_b32_e32 v117, v4
	v_mov_b32_e32 v118, v4
	v_mov_b32_e32 v119, v4
	v_mov_b32_e32 v80, v4
	v_mov_b32_e32 v81, v4
	v_mov_b32_e32 v82, v4
	v_mov_b32_e32 v83, v4
	v_mov_b32_e32 v88, v4
	v_mov_b32_e32 v89, v4
	v_mov_b32_e32 v90, v4
	v_mov_b32_e32 v91, v4
	v_mov_b32_e32 v96, v4
	v_mov_b32_e32 v97, v4
	v_mov_b32_e32 v98, v4
	v_mov_b32_e32 v99, v4
	v_mov_b32_e32 v104, v4
	v_mov_b32_e32 v105, v4
	v_mov_b32_e32 v106, v4
	v_mov_b32_e32 v107, v4
	v_mov_b32_e32 v112, v4
	v_mov_b32_e32 v113, v4
	v_mov_b32_e32 v114, v4
	v_mov_b32_e32 v115, v4
	v_mov_b32_e32 v120, v4
	v_mov_b32_e32 v121, v4
	v_mov_b32_e32 v122, v4
	v_mov_b32_e32 v123, v4
	v_mov_b32_e32 v124, v4
	v_mov_b32_e32 v125, v4
	v_mov_b32_e32 v126, v4
	v_mov_b32_e32 v127, v4
	v_mov_b32_e32 v128, v4
	v_mov_b32_e32 v129, v4
	v_mov_b32_e32 v130, v4
	v_mov_b32_e32 v131, v4
	.p2align 6
